# combine: LN gamma/beta loads hoisted; ln_router: batched image loads; attention: queue atomic wait deferred
# baseline (speedup 1.0000x reference)
; __device__ __forceinline__ float half_max32(float v) { v = row_max16(v); float a; const float b = swap16_other(v, a); return __builtin_fmaxf(a, b); }
; __device__ __forceinline__ float xor32_sum(float v) { float a; const float b = swap32_other(v, a); return a + b; }
; #define GAS __attribute__((address_space(1)))
; #define LAS __attribute__((address_space(3)))
; #define LDS_WAIT() asm volatile("s_waitcnt lgkmcnt(0)" ::: "memory")
; __device__ __forceinline__ void da_attn_phase(Frame& F, const bf16* QKV, bf16* AO, float lam, float one_m_li, const float* subg, const unsigned* kmax, gu32* qctr, const ConvJob& cj) { LTID();
;     ...
;         int tid = tid_; asm volatile("" : "+v"(tid));
;         const int lane = tid & 63, r32 = lane & 31, hh = lane >> 5, wid = __builtin_amdgcn_readfirstlane(tid >> 6), mp = wid & 1, rg = wid >> 1;
;         LAS float* wsf = (LAS float*)(lds + 98304 + wid * 256);
;         const int voff = (4 * hh + ((lane & 15) >> 2)) * 64 + ((lane >> 4) & 1) * 32 + (lane & 3) * 8;
;         unsigned nxtU = 0u; if (tid == 0) nxtU = __hip_atomic_fetch_add(qctr, 1u, RLX_AGENT);
;         const int h = 7 - (U >> 8), qb = 63 - ((U & 255) >> 2), b = U & 3;
;         const int q0 = qb * 128, NT = 2 * qb + 2;
;         const float sl2 = __builtin_amdgcn_exp2f(-(float)(h + 1)) * LOG2E;
;         const size_t rowbase = (size_t)b * SEQ;
;         const unsigned* kmp = kmax + ((b * 16 + h * 2 + mp) * 2);
;         const float km2 = __builtin_bit_cast(float, __hip_atomic_load(kmp, RLX_AGENT)) + __builtin_bit_cast(float, __hip_atomic_load(kmp + 1, RLX_AGENT));
;         bf16x8 qr[4];
;         { const bf16* qp = QKV + (rowbase + q0 + rg * 32 + r32) * 3072 + h * 128 + mp * 64 + hh * 8;
; #pragma unroll
;           for (int d0 = 0; d0 < 4; ++d0) qr[d0] = *(const GAS bf16x8*)(qp + d0 * 16); }
;         int t_min = 0; float qkw = 0.f;
;         { float qs = 0.f;
; #pragma unroll
;           for (int d0 = 0; d0 < 4; ++d0)
; #pragma unroll
;               for (int j = 0; j < 8; ++j) { const float qv = bf2f((unsigned short)qr[d0][j]); qs += qv * qv; }
;           qs = xor32_sum(qs); qs = half_max32(qs);
;           const float bw = 2.0f * sqrtf(qs * km2) * 1.02f;
;           qkw = 0.5f * bw;
;           if (lane == 0) wred[wid] = bw;
;           LDS_WAIT(); __syncthreads();
.LBB0_670:
	v_mov_b32_e32 v238, v240
	v_mov_b32_e32 v239, 0
	v_readfirstlane_b32 s22, v238
	v_cmp_eq_u32_e64 s[4:5], 0, v238
	s_and_saveexec_b64 s[6:7], s[4:5]
	s_cbranch_execz .LBB0_674
	s_mov_b64 s[20:21], exec
	v_mbcnt_lo_u32_b32 v0, s20, 0
	v_mbcnt_hi_u32_b32 v0, s21, v0
	v_cmp_eq_u32_e32 vcc, 0, v0
	s_and_saveexec_b64 s[8:9], vcc
	s_cbranch_execz .LBB0_673
	s_bcnt1_i32_b64 s0, s[20:21]
	v_readlane_b32 s10, v255, 8
	v_mov_b32_e32 v2, s0
	v_readlane_b32 s11, v255, 9
	s_nop 4
	global_atomic_add v239, v1, v2, s[10:11] sc0
.LBB0_673:
	s_or_b64 exec, exec, s[8:9]
.LBB0_674:
	s_or_b64 exec, exec, s[6:7]
	s_ashr_i32 s24, s2, 8
	s_sub_i32 s8, 7, s24
	s_not_b32 s0, s2
	s_and_b32 s2, s2, 3
	s_ashr_i32 s28, s22, 6
	s_lshl_b32 s23, s2, 13
	s_lshl_b32 s2, s2, 4
	s_lshl_b32 s6, s8, 1
	s_and_b32 s61, s28, 1
	s_add_i32 s6, s6, s2
	s_or_b32 s2, s61, s6
	s_bfe_u32 s0, s0, 0x60002
	s_lshl_b32 s78, s2, 1
	s_ashr_i32 s64, s22, 7
	s_lshl_b32 s29, s0, 7
	s_lshl_b64 s[6:7], s[78:79], 2
	s_add_u32 s6, s38, s6
	s_addc_u32 s7, s39, s7
	s_lshl_b32 s60, s64, 5
	s_or_b32 s20, s29, s23
	s_ashr_i32 s2, s60, 31
	v_and_b32_e32 v241, 31, v238
	global_load_dword v4, v1, s[6:7] sc1
	global_load_dword v5, v1, s[6:7] offset:4 sc1
	s_add_u32 s6, s60, s20
	v_or_b32_e32 v0, s6, v241
	v_mov_b64_e32 v[2:3], s[14:15]
	s_movk_i32 s6, 0x1800
	s_addc_u32 s2, s2, 0
	v_mad_u64_u32 v[2:3], s[6:7], v0, s6, v[2:3]
	v_mov_b32_e32 v0, 0x1800
	v_mad_i32_i24 v3, s2, v0, v3
	s_lshl_b32 s78, s8, 8
	v_bfe_u32 v243, v238, 5, 1
	v_lshl_add_u64 v[2:3], v[2:3], 0, s[78:79]
	s_lshl_b32 s78, s61, 7
	v_lshl_add_u64 v[2:3], v[2:3], 0, s[78:79]
	v_lshlrev_b32_e32 v0, 4, v243
	v_lshl_add_u64 v[2:3], v[2:3], 0, v[0:1]
	global_load_dwordx4 v[164:167], v[2:3], off
	global_load_dwordx4 v[168:171], v[2:3], off offset:32
	global_load_dwordx4 v[172:175], v[2:3], off offset:64
	global_load_dwordx4 v[176:179], v[2:3], off offset:96
	v_and_b32_e32 v244, 63, v238
	s_mov_b32 s21, s79
	s_lshl_b32 s30, s8, 7
	s_waitcnt vmcnt(3)
	v_and_b32_e32 v0, 0xffff0000, v164
	v_lshlrev_b32_e32 v2, 16, v164
	v_mul_f32_e32 v0, v0, v0
	v_fmac_f32_e32 v0, v2, v2
	v_lshlrev_b32_e32 v2, 16, v165
	v_fmac_f32_e32 v0, v2, v2
	v_and_b32_e32 v2, 0xffff0000, v165
	v_fmac_f32_e32 v0, v2, v2
	v_lshlrev_b32_e32 v2, 16, v166
	v_fmac_f32_e32 v0, v2, v2
	v_and_b32_e32 v2, 0xffff0000, v166
	v_fmac_f32_e32 v0, v2, v2
	v_lshlrev_b32_e32 v2, 16, v167
	v_fmac_f32_e32 v0, v2, v2
	v_and_b32_e32 v2, 0xffff0000, v167
	v_fmac_f32_e32 v0, v2, v2
	s_waitcnt vmcnt(2)
	v_lshlrev_b32_e32 v2, 16, v168
	v_fmac_f32_e32 v0, v2, v2
	v_and_b32_e32 v2, 0xffff0000, v168
	v_fmac_f32_e32 v0, v2, v2
	v_lshlrev_b32_e32 v2, 16, v169
	v_fmac_f32_e32 v0, v2, v2
	v_and_b32_e32 v2, 0xffff0000, v169
	v_fmac_f32_e32 v0, v2, v2
	v_lshlrev_b32_e32 v2, 16, v170
	v_fmac_f32_e32 v0, v2, v2
	v_and_b32_e32 v2, 0xffff0000, v170
	v_fmac_f32_e32 v0, v2, v2
	v_lshlrev_b32_e32 v2, 16, v171
	v_fmac_f32_e32 v0, v2, v2
	v_and_b32_e32 v2, 0xffff0000, v171
	v_fmac_f32_e32 v0, v2, v2
	s_waitcnt vmcnt(1)
	v_lshlrev_b32_e32 v2, 16, v172
	v_fmac_f32_e32 v0, v2, v2
	v_and_b32_e32 v2, 0xffff0000, v172
	v_fmac_f32_e32 v0, v2, v2
	v_lshlrev_b32_e32 v2, 16, v173
	v_fmac_f32_e32 v0, v2, v2
	v_and_b32_e32 v2, 0xffff0000, v173
	v_fmac_f32_e32 v0, v2, v2
	v_lshlrev_b32_e32 v2, 16, v174
	v_fmac_f32_e32 v0, v2, v2
	v_and_b32_e32 v2, 0xffff0000, v174
	v_fmac_f32_e32 v0, v2, v2
	v_lshlrev_b32_e32 v2, 16, v175
	v_fmac_f32_e32 v0, v2, v2
	v_and_b32_e32 v2, 0xffff0000, v175
	v_fmac_f32_e32 v0, v2, v2
	s_waitcnt vmcnt(0)
	v_lshlrev_b32_e32 v2, 16, v176
	v_fmac_f32_e32 v0, v2, v2
	v_and_b32_e32 v2, 0xffff0000, v176
	v_fmac_f32_e32 v0, v2, v2
	v_lshlrev_b32_e32 v2, 16, v177
	v_fmac_f32_e32 v0, v2, v2
	v_and_b32_e32 v2, 0xffff0000, v177
	v_fmac_f32_e32 v0, v2, v2
	v_lshlrev_b32_e32 v2, 16, v178
	v_fmac_f32_e32 v0, v2, v2
	v_and_b32_e32 v2, 0xffff0000, v178
	v_fmac_f32_e32 v0, v2, v2
	v_lshlrev_b32_e32 v2, 16, v179
	v_fmac_f32_e32 v0, v2, v2
	v_and_b32_e32 v2, 0xffff0000, v179
	v_fmac_f32_e32 v0, v2, v2
	v_mov_b32_e32 v3, v0
	s_nop 1
	v_permlane32_swap_b32 v3, v0
	v_add_f32_e32 v2, v4, v5
	v_add_f32_e32 v0, v0, v3
	s_nop 1
	v_mov_b32_dpp v3, v0 quad_perm:[1,0,3,2] row_mask:0xf bank_mask:0xf bound_ctrl:1
	v_max_f32_e32 v3, v3, v3
	v_max_f32_e32 v0, v0, v3
	s_nop 1
	v_mov_b32_dpp v3, v0 quad_perm:[2,3,0,1] row_mask:0xf bank_mask:0xf bound_ctrl:1
	v_max_f32_e32 v3, v3, v3
	v_max_f32_e32 v0, v0, v3
	s_nop 1
	v_mov_b32_dpp v3, v0 row_half_mirror row_mask:0xf bank_mask:0xf bound_ctrl:1
	v_max_f32_e32 v3, v3, v3
	v_max_f32_e32 v0, v0, v3
	s_nop 1
	v_mov_b32_dpp v3, v0 row_mirror row_mask:0xf bank_mask:0xf bound_ctrl:1
	v_max_f32_e32 v3, v3, v3
	v_max_f32_e32 v0, v0, v3
	v_mov_b32_e32 v3, v0
	s_nop 1
	v_permlane16_swap_b32 v3, v0
	s_nop 0
	v_max_f32_e32 v3, v3, v3
	v_max_f32_e32 v0, v0, v0
	v_max_f32_e32 v0, v0, v3
	v_mul_f32_e32 v0, v2, v0
	v_cmp_gt_f32_e32 vcc, s3, v0
	v_mul_f32_e32 v2, 0x4f800000, v0
	s_nop 0
	v_cndmask_b32_e32 v0, v0, v2, vcc
	v_sqrt_f32_e32 v2, v0
	s_nop 0
	v_add_u32_e32 v3, -1, v2
	v_fma_f32 v4, -v3, v2, v0
	v_cmp_ge_f32_e64 s[6:7], 0, v4
	v_add_u32_e32 v4, 1, v2
	s_nop 0
	v_cndmask_b32_e64 v3, v2, v3, s[6:7]
	v_fma_f32 v2, -v4, v2, v0
	v_cmp_lt_f32_e64 s[6:7], 0, v2
	s_nop 1
	v_cndmask_b32_e64 v2, v3, v4, s[6:7]
	v_mul_f32_e32 v3, 0x37800000, v2
	v_cndmask_b32_e32 v2, v2, v3, vcc
	v_cmp_class_f32_e32 vcc, v0, v229
	v_cmp_eq_u32_e64 s[6:7], 0, v244
	s_nop 0
	v_cndmask_b32_e32 v0, v2, v0, vcc
	v_add_f32_e32 v0, v0, v0
	v_mul_f32_e32 v36, 0x3f828f5c, v0
	s_and_saveexec_b64 s[8:9], s[6:7]
	s_lshl_b32 s2, s28, 2
	s_add_i32 s2, s2, 0
	s_add_i32 s2, s2, 0x21040
	v_mov_b32_e32 v0, s2
	ds_write_b32 v0, v36
	s_or_b64 exec, exec, s[8:9]
	s_sub_i32 s2, 8, s24
	v_cvt_f32_u32_e32 v0, s2
	s_add_i32 s2, 0, 0x21040
	v_mov_b32_e32 v2, s2
	s_waitcnt lgkmcnt(0)
	v_exp_f32_e64 v0, -v0
	s_waitcnt lgkmcnt(0)
	s_barrier
; #define DMA_K(it_, ks) do { const size_t to_ = (size_t)(NT - 1 - (it_)) * 64 * 3072; const unsigned sb_ = (unsigned)(ks) * 16384u; \
;         glds16(kg0 + to_, (unsigned)__builtin_amdgcn_readfirstlane(kd0 + sb_)); glds16(kg0 + to_ + 64, (unsigned)__builtin_amdgcn_readfirstlane(kd0 + sb_ + 8192)); } while (0)
; #define DMA_V(it_, vs) do { const size_t to_ = (size_t)(NT - 1 - (it_)) * 64 * 3072; const unsigned sb_ = (unsigned)(vs) * 16384u; \
;         glds16(vg0 + to_, (unsigned)__builtin_amdgcn_readfirstlane(vd0 + sb_)); glds16(vg0 + to_ + 64, (unsigned)__builtin_amdgcn_readfirstlane(vd0 + sb_ + 8192)); } while (0)
; __device__ __forceinline__ void da_attn_phase(Frame& F, const bf16* QKV, bf16* AO, float lam, float one_m_li, const float* subg, const unsigned* kmax, gu32* qctr, const ConvJob& cj) { LTID();
;     ...
;           float bm = wred[0];
; #pragma unroll
;           for (int w8 = 1; w8 < 8; ++w8) bm = __builtin_fmaxf(bm, wred[w8]);
;           const float Wk = (bm + 38.0f) / sl2, xx = ((float)q0 - Wk - 63.0f) * (1.0f / 64.0f);
;           t_min = (xx > 0.f) ? (int)ceilf(xx) : 0; t_min = __builtin_amdgcn_readfirstlane(t_min); }
;         int NIT = NT - t_min;
;         const bf16* kg0 = QKV + (rowbase + lane) * 3072 + 1024 + h * 128 + wid * 8;
;         const bf16* vg0 = QKV + (rowbase + 16 * (wid & 3) + (lane >> 2)) * 3072 + 2048 + h * 128 + (wid >> 2) * 32 + (lane & 3) * 8;
;         const unsigned ldsb = (unsigned)(uintptr_t)lds, kd0 = ldsb + wid * 1024, vd0 = ldsb + 49152 + (wid >> 2) * 4096 + (wid & 3) * 1024;
;     ...
;         float tmax = -INFINITY;
;         float m_ref = -qkw, l_run = 0.f; f32x16 o[4];
; #pragma unroll
;         for (int eb = 0; eb < 4; ++eb) o[eb] = (f32x16){0.f, 0.f, 0.f, 0.f, 0.f, 0.f, 0.f, 0.f, 0.f, 0.f, 0.f, 0.f, 0.f, 0.f, 0.f, 0.f};
;         const float hb = sl2 * (float)(4 * hh);
;         DMA_K(0, 0); DMA_K(1, 1); DMA_V(0, 0);
;         if (NIT > 2) { DMA_K(2, 2); DMA_V(1, 1); asm volatile("s_waitcnt vmcnt(8)\n\ts_barrier" ::: "memory"); }
;         else { DMA_V(1, 1); asm volatile("s_waitcnt vmcnt(6)\n\ts_barrier" ::: "memory"); }
	ds_read_b128 v[2:5], v2
	v_readlane_b32 s2, v254, 9
	v_mul_f32_e32 v188, 0x3fb8aa3b, v0
	v_cvt_f32_u32_e32 v99, s29
	v_mov_b32_e32 v0, s2
	ds_read_b128 v[6:9], v0
	s_waitcnt lgkmcnt(1)
	v_max_f32_e32 v0, v3, v3
	v_max_f32_e32 v2, v2, v2
	v_max_f32_e32 v0, v2, v0
	v_max3_f32 v0, v0, v4, v5
	s_waitcnt lgkmcnt(0)
	v_max3_f32 v0, v0, v6, v7
	v_max3_f32 v0, v0, v8, v9
	v_add_f32_e32 v0, 0x42180000, v0
	v_div_scale_f32 v2, s[8:9], v188, v188, v0
	v_rcp_f32_e32 v3, v2
	s_bfe_u32 s9, s22, 0x20006
	s_ashr_i32 s22, s22, 8
	s_lshl_b32 s26, s22, 5
	v_fma_f32 v4, -v2, v3, 1.0
	v_fmac_f32_e32 v3, v4, v3
	v_div_scale_f32 v4, vcc, v0, v188, v0
	v_mul_f32_e32 v5, v4, v3
	v_fma_f32 v6, -v2, v5, v4
	v_fmac_f32_e32 v5, v6, v3
	v_fma_f32 v2, -v2, v5, v4
	v_div_fmas_f32 v2, v2, v3, v5
	v_div_fixup_f32 v0, v2, v188, v0
	v_sub_f32_e32 v0, v99, v0
	v_add_f32_e32 v0, 0xc27c0000, v0
	v_mul_f32_e32 v0, 0x3c800000, v0
	v_ceil_f32_e32 v2, v0
	v_cvt_i32_f32_e32 v2, v2
	v_cmp_lt_f32_e32 vcc, 0, v0
	v_lshrrev_b32_e32 v4, 2, v244
	v_lshl_or_b32 v4, s9, 4, v4
	v_cndmask_b32_e32 v0, 0, v2, vcc
	v_or_b32_e32 v4, s23, v4
	v_readfirstlane_b32 s8, v0
	v_or_b32_e32 v0, s23, v244
	v_mul_u32_u24_e32 v0, 0xc00, v0
	s_lshl_b32 s22, s22, 12
	v_lshlrev_b32_e32 v0, 1, v0
	v_mul_u32_u24_e32 v4, 0xc00, v4
	s_add_i32 s22, s22, 0
	s_lshl_b32 s9, s9, 10
	v_lshl_add_u64 v[2:3], s[14:15], 0, v[0:1]
	s_lshl_b32 s24, s28, 3
	v_lshlrev_b32_e32 v34, 1, v4
	v_mov_b32_e32 v35, v1
	s_add_i32 s69, s22, s9
	s_lshl_b32 s22, s30, 1
	s_mov_b32 s23, s79
	v_lshlrev_b32_e32 v124, 3, v238
	s_ashr_i32 s25, s24, 31
	v_lshl_add_u64 v[4:5], s[14:15], 0, v[34:35]
	v_lshl_add_u64 v[2:3], v[2:3], 0, s[22:23]
	s_lshl_b32 s2, s0, 1
	v_and_b32_e32 v37, 24, v124
	s_ashr_i32 s27, s26, 31
	v_lshl_add_u64 v[186:187], s[24:25], 1, v[2:3]
	v_lshl_add_u64 v[2:3], v[4:5], 0, s[22:23]
	s_add_i32 s68, s2, 2
	v_lshl_add_u64 v[2:3], s[26:27], 1, v[2:3]
	v_lshlrev_b32_e32 v4, 1, v37
	v_mov_b32_e32 v5, v1
	s_sub_i32 s70, s68, s8
	v_lshl_add_u64 v[2:3], v[2:3], 0, v[4:5]
	s_mov_b64 s[8:9], 0x1000
	s_or_b32 s71, s2, 1
	v_lshl_add_u64 v[184:185], v[2:3], 0, s[8:9]
	s_mul_i32 s8, s71, 0x60000
	s_mov_b32 s9, s79
	s_lshl_b32 s72, s28, 10
	v_lshl_add_u64 v[2:3], v[186:187], 0, s[8:9]
	s_mov_b64 s[12:13], 0x800
	s_add_i32 s72, s72, 0
	v_lshl_add_u64 v[4:5], v[2:3], 0, s[12:13]
	s_mov_b32 s23, m0
	s_mov_b32 m0, s72
	s_nop 0
	global_load_lds_dwordx4 v[4:5], off
	s_mov_b32 m0, s23
	s_mov_b64 s[34:35], 0x880
	s_add_i32 s23, s72, 0x2000
	v_lshl_add_u64 v[2:3], v[2:3], 0, s[34:35]
	s_mov_b32 s30, m0
	s_mov_b32 m0, s23
	s_nop 0
	global_load_lds_dwordx4 v[2:3], off
	s_mov_b32 m0, s30
	s_mul_i32 s23, s0, 0x60000
	s_lshl_b32 s78, s23, 1
	v_lshl_add_u64 v[4:5], v[186:187], 0, s[78:79]
	v_lshl_add_u64 v[2:3], v[4:5], 0, s[12:13]
	s_add_i32 s23, s72, 0x4000
	s_mov_b32 s30, m0
	s_mov_b32 m0, s23
	s_nop 0
	global_load_lds_dwordx4 v[2:3], off
	s_mov_b32 m0, s30
	v_lshl_add_u64 v[4:5], v[4:5], 0, s[34:35]
	s_add_i32 s23, s72, 0x6000
	s_mov_b32 s30, m0
	s_mov_b32 m0, s23
	s_nop 0
	global_load_lds_dwordx4 v[4:5], off
	s_mov_b32 m0, s30
	s_add_i32 s69, s69, 0xc000
	v_lshl_add_u64 v[4:5], v[184:185], 0, s[8:9]
	s_mov_b32 s8, m0
	s_mov_b32 m0, s69
	s_nop 0
	global_load_lds_dwordx4 v[4:5], off
	s_mov_b32 m0, s8
	v_lshl_add_u64 v[4:5], v[4:5], 0, s[54:55]
	s_add_i32 s8, s69, 0x2000
	s_mov_b32 s9, m0
	s_mov_b32 m0, s8
	s_nop 0
	global_load_lds_dwordx4 v[4:5], off
	s_mov_b32 m0, s9
	s_mov_b64 s[10:11], 0x880
	s_cmp_lt_i32 s70, 3
	s_mov_b64 s[8:9], -1
	s_cbranch_scc0 .LBB0_678
	v_lshl_add_u64 v[4:5], v[184:185], 0, s[78:79]
	s_add_i32 s8, s69, 0x4000
	s_mov_b32 s9, m0
	s_mov_b32 m0, s8
	s_nop 0
	global_load_lds_dwordx4 v[4:5], off
	s_mov_b32 m0, s9
	v_lshl_add_u64 v[4:5], v[4:5], 0, s[54:55]
	s_add_i32 s8, s69, 0x6000
	s_mov_b32 s9, m0
	s_mov_b32 m0, s8
	s_nop 0
	global_load_lds_dwordx4 v[4:5], off
	s_mov_b32 m0, s9
	s_waitcnt vmcnt(6)
	s_barrier
	s_mov_b64 s[8:9], 0
